# baseline (speedup 1.0000x reference)
.LBB3_14:
	v_add_u32_e32 v3, s34, v227
	ds_read_b64_tr_b16 v[210:211], v3 offset:24576
	ds_read_b64_tr_b16 v[212:213], v3 offset:25088
	s_waitcnt lgkmcnt(9)
	v_mfma_f32_32x32x16_f16 v[130:145], v[206:209], v[162:165], v[66:81]
	s_add_u32 s16, s18, s6
	s_addc_u32 s39, s19, s7
	s_add_u32 s64, s16, 0x8000
	s_addc_u32 s65, s39, 0
	s_add_i32 s62, s58, s56
	s_add_u32 s40, s8, s6
	s_addc_u32 s41, s9, s7
	s_mov_b32 s63, m0
	s_mov_b32 m0, s62
	s_nop 0
	global_load_lds_dwordx4 v246, s[64:65]
	s_add_u32 s64, s40, 0x4000
	s_addc_u32 s65, s41, 0
	s_add_i32 s62, s38, s57
	s_mov_b32 m0, s62
	s_nop 0
	global_load_lds_dwordx4 v246, s[64:65]
	s_mov_b32 m0, s63
	v_add_f32_e32 v4, v98, v99
	v_add_f32_e32 v4, v100, v4
	v_add_f32_e32 v4, v101, v4
	v_add_f32_e32 v4, v102, v4
	v_add_f32_e32 v4, v103, v4
	v_cvt_pk_f16_f32 v174, v98, v99
	v_cvt_pk_f16_f32 v175, v100, v101
	ds_read_b64_tr_b16 v[206:207], v3 offset:28672
	ds_read_b64_tr_b16 v[208:209], v3 offset:29184
	s_waitcnt lgkmcnt(10)
	v_mfma_f32_32x32x16_f16 v[114:129], v[202:205], v[162:165], v[66:81]
	v_add_f32_e32 v4, v104, v4
	v_add_f32_e32 v4, v105, v4
	v_add_f32_e32 v4, v106, v4
	v_add_f32_e32 v4, v107, v4
	v_cvt_pk_f16_f32 v176, v102, v103
	v_cvt_pk_f16_f32 v177, v104, v105
	ds_read_b64_tr_b16 v[202:203], v3 offset:25600
	ds_read_b64_tr_b16 v[204:205], v3 offset:26112
	s_waitcnt lgkmcnt(11)
	v_mfma_f32_32x32x16_f16 v[130:145], v[198:201], v[154:157], v[130:145]
	v_add_f32_e32 v4, v108, v4
	v_add_f32_e32 v4, v109, v4
	v_add_f32_e32 v4, v110, v4
	v_add_f32_e32 v4, v111, v4
	v_cvt_pk_f16_f32 v170, v106, v107
	v_cvt_pk_f16_f32 v171, v108, v109
	ds_read_b64_tr_b16 v[102:103], v3 offset:29696
	ds_read_b64_tr_b16 v[104:105], v3 offset:30208
	s_waitcnt lgkmcnt(12)
	v_mfma_f32_32x32x16_f16 v[114:129], v[194:197], v[154:157], v[114:129]
	v_add_f32_e32 v4, v112, v4
	v_add_f32_e32 v4, v113, v4
	v_add_f32_e32 v4, v82, v4
	v_add_f32_e32 v4, v83, v4
	v_cvt_pk_f16_f32 v172, v110, v111
	v_cvt_pk_f16_f32 v173, v112, v113
	ds_read_b64_tr_b16 v[98:99], v3 offset:26624
	ds_read_b64_tr_b16 v[100:101], v3 offset:27136
	s_waitcnt lgkmcnt(13)
	v_mfma_f32_32x32x16_f16 v[130:145], v[190:193], v[150:153], v[130:145]
	v_add_f32_e32 v4, v84, v4
	v_add_f32_e32 v4, v85, v4
	v_add_f32_e32 v4, v86, v4
	v_add_f32_e32 v4, v87, v4
	v_cvt_pk_f16_f32 v166, v82, v83
	v_cvt_pk_f16_f32 v167, v84, v85
	ds_read_b64_tr_b16 v[12:13], v3 offset:30720
	ds_read_b64_tr_b16 v[14:15], v3 offset:31232
	s_waitcnt lgkmcnt(14)
	v_mfma_f32_32x32x16_f16 v[114:129], v[186:189], v[150:153], v[114:129]
	v_add_f32_e32 v4, v88, v4
	v_add_f32_e32 v4, v89, v4
	v_add_f32_e32 v4, v90, v4
	v_add_f32_e32 v4, v91, v4
	v_cvt_pk_f16_f32 v168, v86, v87
	v_cvt_pk_f16_f32 v169, v88, v89
	ds_read_b64_tr_b16 v[8:9], v3 offset:27648
	ds_read_b64_tr_b16 v[10:11], v3 offset:28160
	s_waitcnt lgkmcnt(14)
	v_mfma_f32_32x32x16_f16 v[130:145], v[182:185], v[146:149], v[130:145]
	v_add_f32_e32 v4, v92, v4
	v_add_f32_e32 v4, v93, v4
	v_add_f32_e32 v4, v94, v4
	v_add_f32_e32 v17, v95, v4
	v_cvt_pk_f16_f32 v158, v90, v91
	v_cvt_pk_f16_f32 v159, v92, v93
	ds_read_b64_tr_b16 v[4:5], v3 offset:31744
	ds_read_b64_tr_b16 v[6:7], v3 offset:32256
	v_mfma_f32_32x32x16_f16 v[114:129], v[178:181], v[146:149], v[114:129]
	v_add_f32_e32 v3, v96, v17
	v_add_f32_e32 v3, v97, v3
	v_add_f32_e32 v3, 0, v3
	v_cvt_pk_f16_f32 v160, v94, v95
	v_cvt_pk_f16_f32 v161, v96, v97
	s_andn2_b64 vcc, exec, s[28:29]
	s_cbranch_vccnz .LBB3_16
	s_waitcnt vmcnt(0)
	s_nop 0
	v_bfe_u32 v83, v224, v231, 1
	v_lshrrev_b32_e32 v17, v231, v224
	v_cmp_eq_u32_e32 vcc, 0, v83
	v_bfe_u32 v83, v225, v231, 1
	v_lshrrev_b32_e32 v82, v231, v225
	v_cndmask_b32_e32 v130, v242, v130, vcc
	v_cmp_eq_u32_e32 vcc, 0, v83
	v_and_b32_e32 v83, 2, v17
	s_nop 0
	v_cndmask_b32_e32 v114, v242, v114, vcc
	v_cmp_eq_u32_e32 vcc, 0, v83
	v_and_b32_e32 v83, 2, v82
	s_nop 0
	v_cndmask_b32_e32 v131, v242, v131, vcc
	v_cmp_eq_u32_e32 vcc, 0, v83
	v_and_b32_e32 v83, 4, v17
	s_nop 0
	v_cndmask_b32_e32 v115, v242, v115, vcc
	v_cmp_eq_u32_e32 vcc, 0, v83
	v_and_b32_e32 v83, 4, v82
	s_nop 0
	v_cndmask_b32_e32 v132, v242, v132, vcc
	v_cmp_eq_u32_e32 vcc, 0, v83
	v_and_b32_e32 v83, 8, v17
	s_nop 0
	v_cndmask_b32_e32 v116, v242, v116, vcc
	v_cmp_eq_u32_e32 vcc, 0, v83
	v_and_b32_e32 v83, 8, v82
	s_nop 0
	v_cndmask_b32_e32 v133, v242, v133, vcc
	v_cmp_eq_u32_e32 vcc, 0, v83
	v_and_b32_e32 v83, 0x100, v17
	s_nop 0
	v_cndmask_b32_e32 v117, v242, v117, vcc
	v_cmp_eq_u32_e32 vcc, 0, v83
	v_and_b32_e32 v83, 0x100, v82
	s_nop 0
	v_cndmask_b32_e32 v134, v242, v134, vcc
	v_cmp_eq_u32_e32 vcc, 0, v83
	v_and_b32_e32 v83, 0x200, v17
	s_nop 0
	v_cndmask_b32_e32 v118, v242, v118, vcc
	v_cmp_eq_u32_e32 vcc, 0, v83
	v_and_b32_e32 v83, 0x200, v82
	s_nop 0
	v_cndmask_b32_e32 v135, v242, v135, vcc
	v_cmp_eq_u32_e32 vcc, 0, v83
	v_and_b32_e32 v83, 0x400, v17
	s_nop 0
	v_cndmask_b32_e32 v119, v242, v119, vcc
	v_cmp_eq_u32_e32 vcc, 0, v83
	v_and_b32_e32 v83, 0x400, v82
	s_nop 0
	v_cndmask_b32_e32 v136, v242, v136, vcc
	v_cmp_eq_u32_e32 vcc, 0, v83
	v_and_b32_e32 v83, 0x800, v17
	s_nop 0
	v_cndmask_b32_e32 v120, v242, v120, vcc
	v_cmp_eq_u32_e32 vcc, 0, v83
	v_and_b32_e32 v83, 0x800, v82
	s_nop 0
	v_cndmask_b32_e32 v137, v242, v137, vcc
	v_cmp_eq_u32_e32 vcc, 0, v83
	v_and_b32_e32 v83, 0x10000, v17
	s_nop 0
	v_cndmask_b32_e32 v121, v242, v121, vcc
	v_cmp_eq_u32_e32 vcc, 0, v83
	v_and_b32_e32 v83, 0x10000, v82
	s_nop 0
	v_cndmask_b32_e32 v138, v242, v138, vcc
	v_cmp_eq_u32_e32 vcc, 0, v83
	v_and_b32_e32 v83, 0x20000, v17
	s_nop 0
	v_cndmask_b32_e32 v122, v242, v122, vcc
	v_cmp_eq_u32_e32 vcc, 0, v83
	v_and_b32_e32 v83, 0x20000, v82
	s_nop 0
	v_cndmask_b32_e32 v139, v242, v139, vcc
	v_cmp_eq_u32_e32 vcc, 0, v83
	v_and_b32_e32 v83, 0x40000, v17
	s_nop 0
	v_cndmask_b32_e32 v123, v242, v123, vcc
	v_cmp_eq_u32_e32 vcc, 0, v83
	v_and_b32_e32 v83, 0x40000, v82
	s_nop 0
	v_cndmask_b32_e32 v140, v242, v140, vcc
	v_cmp_eq_u32_e32 vcc, 0, v83
	v_and_b32_e32 v83, 0x80000, v17
	s_nop 0
	v_cndmask_b32_e32 v124, v242, v124, vcc
	v_cmp_eq_u32_e32 vcc, 0, v83
	v_and_b32_e32 v83, 0x80000, v82
	s_nop 0
	v_cndmask_b32_e32 v141, v242, v141, vcc
	v_cmp_eq_u32_e32 vcc, 0, v83
	v_and_b32_e32 v83, 0x1000000, v17
	s_nop 0
	v_cndmask_b32_e32 v125, v242, v125, vcc
	v_cmp_eq_u32_e32 vcc, 0, v83
	v_and_b32_e32 v83, 0x1000000, v82
	s_nop 0
	v_cndmask_b32_e32 v142, v242, v142, vcc
	v_cmp_eq_u32_e32 vcc, 0, v83
	v_and_b32_e32 v83, 0x2000000, v17
	s_nop 0
	v_cndmask_b32_e32 v126, v242, v126, vcc
	v_cmp_eq_u32_e32 vcc, 0, v83
	v_and_b32_e32 v83, 0x2000000, v82
	s_nop 0
	v_cndmask_b32_e32 v143, v242, v143, vcc
	v_cmp_eq_u32_e32 vcc, 0, v83
	v_and_b32_e32 v83, 0x4000000, v17
	v_and_b32_e32 v17, 0x8000000, v17
	v_cndmask_b32_e32 v127, v242, v127, vcc
	v_cmp_eq_u32_e32 vcc, 0, v83
	v_and_b32_e32 v83, 0x4000000, v82
	s_nop 0
	v_cndmask_b32_e32 v144, v242, v144, vcc
	v_cmp_eq_u32_e32 vcc, 0, v83
	s_nop 1
	v_cndmask_b32_e32 v128, v242, v128, vcc
	v_cmp_eq_u32_e32 vcc, 0, v17
	v_and_b32_e32 v17, 0x8000000, v82
	s_nop 0
	v_cndmask_b32_e32 v145, v242, v145, vcc
	v_cmp_eq_u32_e32 vcc, 0, v17
	s_nop 1
	v_cndmask_b32_e32 v129, v242, v129, vcc
.LBB3_16:
	v_max_f32_e32 v17, v131, v131
	v_max_f32_e32 v82, v130, v130
	v_max_f32_e32 v17, v82, v17
	s_nop 1
	v_max3_f32 v82, v132, v133, v115
	v_max3_f32 v17, v17, v114, v116
	v_max3_f32 v17, v17, v117, v134
	v_max3_f32 v82, v82, v136, v137
	v_max3_f32 v17, v17, v135, v118
	v_max3_f32 v82, v82, v120, v121
	v_max3_f32 v17, v17, v119, v138
	v_max3_f32 v82, v82, v140, v141
	v_max3_f32 v17, v17, v139, v122
	v_max3_f32 v82, v82, v124, v125
	v_max3_f32 v17, v17, v123, v142
	v_max3_f32 v82, v82, v144, v145
	v_max3_f32 v17, v17, v143, v126
	v_max3_f32 v82, v82, v128, v129
	v_max3_f32 v17, v17, v127, v82
	v_mov_b32_e32 v82, v17
	s_nop 0
	v_permlane32_swap_b32_e32 v17, v82
	v_max_f32_e32 v82, v82, v82
	v_max_f32_e32 v17, v17, v17
	v_max_f32_e32 v17, v17, v82
	v_cmp_lt_f32_e32 vcc, s50, v17
	s_cmp_lg_u64 vcc, 0
	v_add_f32_e32 v3, v247, v3
	s_cselect_b64 s[28:29], -1, 0
	s_cbranch_vccnz .LBB3_28

.LBB3_21:
	v_add_u32_e32 v6, s58, v227
	ds_read_b64_tr_b16 v[186:187], v6 offset:24576
	ds_read_b64_tr_b16 v[188:189], v6 offset:25088
	s_waitcnt lgkmcnt(9)
	v_mfma_f32_32x32x16_f16 v[98:113], v[82:85], v[162:165], v[66:81]
	s_add_i32 s62, s38, 0x2000
	s_cmpk_lg_i32 s38, 0x4000
	s_cselect_b32 s58, s62, 0
	s_add_u32 s64, s16, 0xa000
	s_addc_u32 s65, s39, 0
	s_add_i32 s62, s38, s56
	s_mov_b32 s63, m0
	s_mov_b32 m0, s62
	s_nop 0
	global_load_lds_dwordx4 v246, s[64:65]
	s_add_u32 s64, s40, 0x6000
	s_addc_u32 s65, s41, 0
	s_add_i32 s62, s58, s57
	s_mov_b32 m0, s62
	s_nop 0
	global_load_lds_dwordx4 v246, s[64:65]
	s_mov_b32 m0, s63
	v_add_f32_e32 v4, v130, v131
	v_add_f32_e32 v4, v132, v4
	v_add_f32_e32 v4, v133, v4
	v_add_f32_e32 v4, v134, v4
	v_add_f32_e32 v4, v135, v4
	v_cvt_pk_f16_f32 v174, v130, v131
	v_cvt_pk_f16_f32 v175, v132, v133
	ds_read_b64_tr_b16 v[182:183], v6 offset:28672
	ds_read_b64_tr_b16 v[184:185], v6 offset:29184
	s_waitcnt lgkmcnt(10)
	v_mfma_f32_32x32x16_f16 v[82:97], v[178:181], v[162:165], v[66:81]
	v_add_f32_e32 v4, v136, v4
	v_add_f32_e32 v4, v137, v4
	v_add_f32_e32 v4, v138, v4
	v_add_f32_e32 v4, v139, v4
	v_cvt_pk_f16_f32 v176, v134, v135
	v_cvt_pk_f16_f32 v177, v136, v137
	ds_read_b64_tr_b16 v[178:179], v6 offset:25600
	ds_read_b64_tr_b16 v[180:181], v6 offset:26112
	s_waitcnt lgkmcnt(11)
	v_mfma_f32_32x32x16_f16 v[98:113], v[210:213], v[154:157], v[98:113]
	v_add_f32_e32 v4, v140, v4
	v_add_f32_e32 v4, v141, v4
	v_add_f32_e32 v4, v142, v4
	v_add_f32_e32 v4, v143, v4
	v_cvt_pk_f16_f32 v170, v138, v139
	v_cvt_pk_f16_f32 v171, v140, v141
	ds_read_b64_tr_b16 v[134:135], v6 offset:29696
	ds_read_b64_tr_b16 v[136:137], v6 offset:30208
	s_waitcnt lgkmcnt(12)
	v_mfma_f32_32x32x16_f16 v[82:97], v[202:205], v[154:157], v[82:97]
	v_add_f32_e32 v4, v144, v4
	v_add_f32_e32 v4, v145, v4
	v_add_f32_e32 v4, v114, v4
	v_add_f32_e32 v4, v115, v4
	v_cvt_pk_f16_f32 v172, v142, v143
	v_cvt_pk_f16_f32 v173, v144, v145
	ds_read_b64_tr_b16 v[130:131], v6 offset:26624
	ds_read_b64_tr_b16 v[132:133], v6 offset:27136
	s_waitcnt lgkmcnt(13)
	v_mfma_f32_32x32x16_f16 v[98:113], v[206:209], v[150:153], v[98:113]
	v_add_f32_e32 v4, v116, v4
	v_add_f32_e32 v4, v117, v4
	v_add_f32_e32 v4, v118, v4
	v_add_f32_e32 v4, v119, v4
	v_cvt_pk_f16_f32 v166, v114, v115
	v_cvt_pk_f16_f32 v167, v116, v117
	ds_read_b64_tr_b16 v[12:13], v6 offset:30720
	ds_read_b64_tr_b16 v[14:15], v6 offset:31232
	s_waitcnt lgkmcnt(14)
	v_mfma_f32_32x32x16_f16 v[82:97], v[194:197], v[150:153], v[82:97]
	v_add_f32_e32 v4, v120, v4
	v_add_f32_e32 v4, v121, v4
	v_add_f32_e32 v4, v122, v4
	v_add_f32_e32 v4, v123, v4
	v_cvt_pk_f16_f32 v168, v118, v119
	v_cvt_pk_f16_f32 v169, v120, v121
	ds_read_b64_tr_b16 v[8:9], v6 offset:27648
	ds_read_b64_tr_b16 v[10:11], v6 offset:28160
	s_waitcnt lgkmcnt(14)
	v_mfma_f32_32x32x16_f16 v[98:113], v[198:201], v[146:149], v[98:113]
	v_add_f32_e32 v4, v124, v4
	v_add_f32_e32 v4, v125, v4
	v_add_f32_e32 v4, v126, v4
	v_add_f32_e32 v17, v127, v4
	v_cvt_pk_f16_f32 v158, v122, v123
	v_cvt_pk_f16_f32 v159, v124, v125
	ds_read_b64_tr_b16 v[4:5], v6 offset:31744
	ds_read_b64_tr_b16 v[6:7], v6 offset:32256
	v_mfma_f32_32x32x16_f16 v[82:97], v[190:193], v[146:149], v[82:97]
	v_add_f32_e32 v17, v128, v17
	v_add_f32_e32 v17, v129, v17
	v_add_f32_e32 v17, 0, v17
	v_cvt_pk_f16_f32 v160, v126, v127
	v_cvt_pk_f16_f32 v161, v128, v129
	s_andn2_b64 vcc, exec, s[28:29]
	s_cbranch_vccnz .LBB3_23
	s_waitcnt vmcnt(0)
	s_nop 0
	v_bfe_u32 v116, v224, v231, 1
	v_lshrrev_b32_e32 v114, v231, v224
	v_cmp_eq_u32_e32 vcc, 0, v116
	v_bfe_u32 v116, v225, v231, 1
	v_lshrrev_b32_e32 v115, v231, v225
	v_cndmask_b32_e32 v98, v242, v98, vcc
	v_cmp_eq_u32_e32 vcc, 0, v116
	v_and_b32_e32 v116, 2, v114
	s_nop 0
	v_cndmask_b32_e32 v82, v242, v82, vcc
	v_cmp_eq_u32_e32 vcc, 0, v116
	v_and_b32_e32 v116, 2, v115
	s_nop 0
	v_cndmask_b32_e32 v99, v242, v99, vcc
	v_cmp_eq_u32_e32 vcc, 0, v116
	v_and_b32_e32 v116, 4, v114
	s_nop 0
	v_cndmask_b32_e32 v83, v242, v83, vcc
	v_cmp_eq_u32_e32 vcc, 0, v116
	v_and_b32_e32 v116, 4, v115
	s_nop 0
	v_cndmask_b32_e32 v100, v242, v100, vcc
	v_cmp_eq_u32_e32 vcc, 0, v116
	v_and_b32_e32 v116, 8, v114
	s_nop 0
	v_cndmask_b32_e32 v84, v242, v84, vcc
	v_cmp_eq_u32_e32 vcc, 0, v116
	v_and_b32_e32 v116, 8, v115
	s_nop 0
	v_cndmask_b32_e32 v101, v242, v101, vcc
	v_cmp_eq_u32_e32 vcc, 0, v116
	v_and_b32_e32 v116, 0x100, v114
	s_nop 0
	v_cndmask_b32_e32 v85, v242, v85, vcc
	v_cmp_eq_u32_e32 vcc, 0, v116
	v_and_b32_e32 v116, 0x100, v115
	s_nop 0
	v_cndmask_b32_e32 v102, v242, v102, vcc
	v_cmp_eq_u32_e32 vcc, 0, v116
	v_and_b32_e32 v116, 0x200, v114
	s_nop 0
	v_cndmask_b32_e32 v86, v242, v86, vcc
	v_cmp_eq_u32_e32 vcc, 0, v116
	v_and_b32_e32 v116, 0x200, v115
	s_nop 0
	v_cndmask_b32_e32 v103, v242, v103, vcc
	v_cmp_eq_u32_e32 vcc, 0, v116
	v_and_b32_e32 v116, 0x400, v114
	s_nop 0
	v_cndmask_b32_e32 v87, v242, v87, vcc
	v_cmp_eq_u32_e32 vcc, 0, v116
	v_and_b32_e32 v116, 0x400, v115
	s_nop 0
	v_cndmask_b32_e32 v104, v242, v104, vcc
	v_cmp_eq_u32_e32 vcc, 0, v116
	v_and_b32_e32 v116, 0x800, v114
	s_nop 0
	v_cndmask_b32_e32 v88, v242, v88, vcc
	v_cmp_eq_u32_e32 vcc, 0, v116
	v_and_b32_e32 v116, 0x800, v115
	s_nop 0
	v_cndmask_b32_e32 v105, v242, v105, vcc
	v_cmp_eq_u32_e32 vcc, 0, v116
	v_and_b32_e32 v116, 0x10000, v114
	s_nop 0
	v_cndmask_b32_e32 v89, v242, v89, vcc
	v_cmp_eq_u32_e32 vcc, 0, v116
	v_and_b32_e32 v116, 0x10000, v115
	s_nop 0
	v_cndmask_b32_e32 v106, v242, v106, vcc
	v_cmp_eq_u32_e32 vcc, 0, v116
	v_and_b32_e32 v116, 0x20000, v114
	s_nop 0
	v_cndmask_b32_e32 v90, v242, v90, vcc
	v_cmp_eq_u32_e32 vcc, 0, v116
	v_and_b32_e32 v116, 0x20000, v115
	s_nop 0
	v_cndmask_b32_e32 v107, v242, v107, vcc
	v_cmp_eq_u32_e32 vcc, 0, v116
	v_and_b32_e32 v116, 0x40000, v114
	s_nop 0
	v_cndmask_b32_e32 v91, v242, v91, vcc
	v_cmp_eq_u32_e32 vcc, 0, v116
	v_and_b32_e32 v116, 0x40000, v115
	s_nop 0
	v_cndmask_b32_e32 v108, v242, v108, vcc
	v_cmp_eq_u32_e32 vcc, 0, v116
	v_and_b32_e32 v116, 0x80000, v114
	s_nop 0
	v_cndmask_b32_e32 v92, v242, v92, vcc
	v_cmp_eq_u32_e32 vcc, 0, v116
	v_and_b32_e32 v116, 0x80000, v115
	s_nop 0
	v_cndmask_b32_e32 v109, v242, v109, vcc
	v_cmp_eq_u32_e32 vcc, 0, v116
	v_and_b32_e32 v116, 0x1000000, v114
	s_nop 0
	v_cndmask_b32_e32 v93, v242, v93, vcc
	v_cmp_eq_u32_e32 vcc, 0, v116
	v_and_b32_e32 v116, 0x1000000, v115
	s_nop 0
	v_cndmask_b32_e32 v110, v242, v110, vcc
	v_cmp_eq_u32_e32 vcc, 0, v116
	v_and_b32_e32 v116, 0x2000000, v114
	s_nop 0
	v_cndmask_b32_e32 v94, v242, v94, vcc
	v_cmp_eq_u32_e32 vcc, 0, v116
	v_and_b32_e32 v116, 0x2000000, v115
	s_nop 0
	v_cndmask_b32_e32 v111, v242, v111, vcc
	v_cmp_eq_u32_e32 vcc, 0, v116
	v_and_b32_e32 v116, 0x4000000, v114
	v_and_b32_e32 v114, 0x8000000, v114
	v_cndmask_b32_e32 v95, v242, v95, vcc
	v_cmp_eq_u32_e32 vcc, 0, v116
	v_and_b32_e32 v116, 0x4000000, v115
	s_nop 0
	v_cndmask_b32_e32 v112, v242, v112, vcc
	v_cmp_eq_u32_e32 vcc, 0, v116
	s_nop 1
	v_cndmask_b32_e32 v96, v242, v96, vcc
	v_cmp_eq_u32_e32 vcc, 0, v114
	v_and_b32_e32 v114, 0x8000000, v115
	s_nop 0
	v_cndmask_b32_e32 v113, v242, v113, vcc
	v_cmp_eq_u32_e32 vcc, 0, v114
	s_nop 1
	v_cndmask_b32_e32 v97, v242, v97, vcc
.LBB3_23:
	v_add_f32_e32 v247, v3, v17
	v_max_f32_e32 v3, v99, v99
	v_max_f32_e32 v17, v98, v98
	v_max_f32_e32 v3, v17, v3
	s_nop 0
	v_max3_f32 v17, v100, v101, v83
	v_max3_f32 v3, v3, v82, v84
	v_max3_f32 v3, v3, v85, v102
	v_max3_f32 v17, v17, v104, v105
	v_max3_f32 v3, v3, v103, v86
	v_max3_f32 v17, v17, v88, v89
	v_max3_f32 v3, v3, v87, v106
	v_max3_f32 v17, v17, v108, v109
	v_max3_f32 v3, v3, v107, v90
	v_max3_f32 v17, v17, v92, v93
	v_max3_f32 v3, v3, v91, v110
	v_max3_f32 v17, v17, v112, v113
	v_max3_f32 v3, v3, v111, v94
	v_max3_f32 v17, v17, v96, v97
	v_max3_f32 v3, v3, v95, v17
	v_mov_b32_e32 v17, v3
	v_permlane32_swap_b32_e32 v3, v17
	v_max_f32_e32 v17, v17, v17
	v_max_f32_e32 v3, v3, v3
	v_max_f32_e32 v3, v3, v17
	v_cmp_lt_f32_e32 vcc, s50, v3
	s_cmp_lg_u64 vcc, 0
	s_cselect_b64 s[28:29], -1, 0
	s_cbranch_vccnz .LBB3_31

	.amdhsa_kernel _Z11attn_kernelPKDF16_S0_S0_PDF16_PKjS3_
		.amdhsa_group_segment_fixed_size 0
		.amdhsa_private_segment_fixed_size 0
		.amdhsa_kernarg_size 48
		.amdhsa_user_sgpr_count 2
		.amdhsa_user_sgpr_dispatch_ptr 0
		.amdhsa_user_sgpr_queue_ptr 0
		.amdhsa_user_sgpr_kernarg_segment_ptr 1
		.amdhsa_user_sgpr_dispatch_id 0
		.amdhsa_user_sgpr_kernarg_preload_length 0
		.amdhsa_user_sgpr_kernarg_preload_offset 0
		.amdhsa_user_sgpr_private_segment_size 0
		.amdhsa_uses_dynamic_stack 0
		.amdhsa_enable_private_segment 0
		.amdhsa_system_sgpr_workgroup_id_x 1
		.amdhsa_system_sgpr_workgroup_id_y 0
		.amdhsa_system_sgpr_workgroup_id_z 0
		.amdhsa_system_sgpr_workgroup_info 0
		.amdhsa_system_vgpr_workitem_id 0
		.amdhsa_next_free_vgpr 248
		.amdhsa_next_free_sgpr 66
		.amdhsa_accum_offset 248
		.amdhsa_reserve_vcc 1
		.amdhsa_float_round_mode_32 0
		.amdhsa_float_round_mode_16_64 0
		.amdhsa_float_denorm_mode_32 3
		.amdhsa_float_denorm_mode_16_64 3
		.amdhsa_dx10_clamp 1
		.amdhsa_ieee_mode 1
		.amdhsa_fp16_overflow 0
		.amdhsa_tg_split 0
		.amdhsa_exception_fp_ieee_invalid_op 0
		.amdhsa_exception_fp_denorm_src 0
		.amdhsa_exception_fp_ieee_div_zero 0
		.amdhsa_exception_fp_ieee_overflow 0
		.amdhsa_exception_fp_ieee_underflow 0
		.amdhsa_exception_fp_ieee_inexact 0
		.amdhsa_exception_int_div_zero 0
	.end_amdhsa_kernel

amdhsa.kernels:
  - .agpr_count:     0
    .args:
      - .actual_access:  read_only
        .address_space:  global
        .offset:         0
        .size:           8
        .value_kind:     global_buffer
      - .actual_access:  read_only
        .address_space:  global
        .offset:         8
        .size:           8
        .value_kind:     global_buffer
      - .actual_access:  read_only
        .address_space:  global
        .offset:         16
        .size:           8
        .value_kind:     global_buffer
      - .actual_access:  write_only
        .address_space:  global
        .offset:         24
        .size:           8
        .value_kind:     global_buffer
      - .actual_access:  write_only
        .address_space:  global
        .offset:         32
        .size:           8
        .value_kind:     global_buffer
      - .actual_access:  write_only
        .address_space:  global
        .offset:         40
        .size:           8
        .value_kind:     global_buffer
      - .actual_access:  write_only
        .address_space:  global
        .offset:         48
        .size:           8
        .value_kind:     global_buffer
    .group_segment_fixed_size: 0
    .kernarg_segment_align: 8
    .kernarg_segment_size: 56
    .language:       OpenCL C
    .language_version:
      - 2
      - 0
    .max_flat_workgroup_size: 1024
    .name:           _Z11prep_kernelPKfS0_PKiPDF16_S3_PfS4_
    .private_segment_fixed_size: 0
    .sgpr_count:     24
    .sgpr_spill_count: 0
    .symbol:         _Z11prep_kernelPKfS0_PKiPDF16_S3_PfS4_.kd
    .uniform_work_group_size: 1
    .uses_dynamic_stack: false
    .vgpr_count:     40
    .vgpr_spill_count: 0
    .wavefront_size: 64
  - .agpr_count:     0
    .args:
      - .address_space:  global
        .offset:         0
        .size:           8
        .value_kind:     global_buffer
      - .address_space:  global
        .offset:         8
        .size:           8
        .value_kind:     global_buffer
      - .address_space:  global
        .offset:         16
        .size:           8
        .value_kind:     global_buffer
      - .address_space:  global
        .offset:         24
        .size:           8
        .value_kind:     global_buffer
      - .address_space:  global
        .offset:         32
        .size:           8
        .value_kind:     global_buffer
      - .address_space:  global
        .offset:         40
        .size:           8
        .value_kind:     global_buffer
      - .address_space:  global
        .offset:         48
        .size:           8
        .value_kind:     global_buffer
      - .address_space:  global
        .offset:         56
        .size:           8
        .value_kind:     global_buffer
      - .address_space:  global
        .offset:         64
        .size:           8
        .value_kind:     global_buffer
      - .address_space:  global
        .offset:         72
        .size:           8
        .value_kind:     global_buffer
      - .address_space:  global
        .offset:         80
        .size:           8
        .value_kind:     global_buffer
      - .address_space:  global
        .offset:         88
        .size:           8
        .value_kind:     global_buffer
      - .address_space:  global
        .offset:         96
        .size:           8
        .value_kind:     global_buffer
      - .address_space:  global
        .offset:         104
        .size:           8
        .value_kind:     global_buffer
    .group_segment_fixed_size: 0
    .kernarg_segment_align: 8
    .kernarg_segment_size: 112
    .language:       OpenCL C
    .language_version:
      - 2
      - 0
    .max_flat_workgroup_size: 512
    .name:           _Z15gemm_qkv_kernelPKDF16_S0_PDF16_S1_S1_PKfS3_S3_S3_S3_S1_PKiPyPj
    .private_segment_fixed_size: 0
    .sgpr_count:     90
    .sgpr_spill_count: 0
    .symbol:         _Z15gemm_qkv_kernelPKDF16_S0_PDF16_S1_S1_PKfS3_S3_S3_S3_S1_PKiPyPj.kd
    .uniform_work_group_size: 1
    .uses_dynamic_stack: false
    .vgpr_count:     244
    .vgpr_spill_count: 0
    .wavefront_size: 64
  - .agpr_count:     0
    .args:
      - .address_space:  global
        .offset:         0
        .size:           8
        .value_kind:     global_buffer
      - .address_space:  global
        .offset:         8
        .size:           8
        .value_kind:     global_buffer
      - .address_space:  global
        .offset:         16
        .size:           8
        .value_kind:     global_buffer
    .group_segment_fixed_size: 0
    .kernarg_segment_align: 8
    .kernarg_segment_size: 24
    .language:       OpenCL C
    .language_version:
      - 2
      - 0
    .max_flat_workgroup_size: 512
    .name:           _Z15gemm_out_kernelPKDF16_S0_Pf
    .private_segment_fixed_size: 0
    .sgpr_count:     26
    .sgpr_spill_count: 0
    .symbol:         _Z15gemm_out_kernelPKDF16_S0_Pf.kd
    .uniform_work_group_size: 1
    .uses_dynamic_stack: false
    .vgpr_count:     148
    .vgpr_spill_count: 0
    .wavefront_size: 64
  - .agpr_count:     0
    .args:
      - .address_space:  global
        .offset:         0
        .size:           8
        .value_kind:     global_buffer
      - .address_space:  global
        .offset:         8
        .size:           8
        .value_kind:     global_buffer
      - .address_space:  global
        .offset:         16
        .size:           8
        .value_kind:     global_buffer
      - .address_space:  global
        .offset:         24
        .size:           8
        .value_kind:     global_buffer
      - .address_space:  global
        .offset:         32
        .size:           8
        .value_kind:     global_buffer
      - .address_space:  global
        .offset:         40
        .size:           8
        .value_kind:     global_buffer
    .group_segment_fixed_size: 0
    .kernarg_segment_align: 8
    .kernarg_segment_size: 48
    .language:       OpenCL C
    .language_version:
      - 2
      - 0
    .max_flat_workgroup_size: 512
    .name:           _Z11attn_kernelPKDF16_S0_S0_PDF16_PKjS3_
    .private_segment_fixed_size: 0
    .sgpr_count:     72
    .sgpr_spill_count: 0
    .symbol:         _Z11attn_kernelPKDF16_S0_S0_PDF16_PKjS3_.kd
    .uniform_work_group_size: 1
    .uses_dynamic_stack: false
    .vgpr_count:     248
    .vgpr_spill_count: 0
    .wavefront_size: 64
